# int8 GEMM epilogues (gate, MoE up, dense up): accumulator i32-to-f32 conversions issued ahead of the scale/bias wait instead of behind it (pure reordering)
# speedup vs baseline: 1.0024x; 1.0024x over previous
.LBB0_198:
	v_cvt_f32_i32_e32 v119, v119
	v_cvt_f32_i32_e32 v118, v118
	v_cvt_f32_i32_e32 v115, v115
	v_cvt_f32_i32_e32 v114, v114
	v_cvt_f32_i32_e32 v121, v121
	v_cvt_f32_i32_e32 v120, v120
	v_cvt_f32_i32_e32 v117, v117
	v_cvt_f32_i32_e32 v116, v116
	v_cvt_f32_i32_e32 v103, v103
	v_cvt_f32_i32_e32 v102, v102
	v_cvt_f32_i32_e32 v99, v99
	v_cvt_f32_i32_e32 v98, v98
	v_cvt_f32_i32_e32 v105, v105
	v_cvt_f32_i32_e32 v104, v104
	v_cvt_f32_i32_e32 v101, v101
	v_cvt_f32_i32_e32 v100, v100
	v_cvt_f32_i32_e32 v87, v87
	v_cvt_f32_i32_e32 v86, v86
	v_cvt_f32_i32_e32 v83, v83
	v_cvt_f32_i32_e32 v82, v82
	v_cvt_f32_i32_e32 v89, v89
	v_cvt_f32_i32_e32 v88, v88
	v_cvt_f32_i32_e32 v85, v85
	v_cvt_f32_i32_e32 v84, v84
	v_cvt_f32_i32_e32 v71, v71
	v_cvt_f32_i32_e32 v70, v70
	v_cvt_f32_i32_e32 v67, v67
	v_cvt_f32_i32_e32 v66, v66
	v_cvt_f32_i32_e32 v73, v73
	v_cvt_f32_i32_e32 v72, v72
	v_cvt_f32_i32_e32 v69, v69
	v_cvt_f32_i32_e32 v68, v68
	v_cvt_f32_i32_e32 v63, v63
	v_cvt_f32_i32_e32 v62, v62
	v_cvt_f32_i32_e32 v59, v59
	v_cvt_f32_i32_e32 v58, v58
	v_cvt_f32_i32_e32 v55, v55
	v_cvt_f32_i32_e32 v54, v54
	v_cvt_f32_i32_e32 v51, v51
	v_cvt_f32_i32_e32 v50, v50
	v_cvt_f32_i32_e32 v65, v65
	v_cvt_f32_i32_e32 v64, v64
	v_cvt_f32_i32_e32 v61, v61
	v_cvt_f32_i32_e32 v60, v60
	v_cvt_f32_i32_e32 v57, v57
	v_cvt_f32_i32_e32 v56, v56
	v_cvt_f32_i32_e32 v53, v53
	v_cvt_f32_i32_e32 v52, v52
	v_cvt_f32_i32_e32 v47, v47
	v_cvt_f32_i32_e32 v46, v46
	v_cvt_f32_i32_e32 v43, v43
	v_cvt_f32_i32_e32 v42, v42
	v_cvt_f32_i32_e32 v39, v39
	v_cvt_f32_i32_e32 v38, v38
	v_cvt_f32_i32_e32 v35, v35
	v_cvt_f32_i32_e32 v34, v34
	v_cvt_f32_i32_e32 v49, v49
	v_cvt_f32_i32_e32 v48, v48
	v_cvt_f32_i32_e32 v45, v45
	v_cvt_f32_i32_e32 v44, v44
	v_cvt_f32_i32_e32 v41, v41
	v_cvt_f32_i32_e32 v40, v40
	v_cvt_f32_i32_e32 v37, v37
	v_cvt_f32_i32_e32 v36, v36
	v_cvt_f32_i32_e32 v31, v31
	v_cvt_f32_i32_e32 v30, v30
	v_cvt_f32_i32_e32 v27, v27
	v_cvt_f32_i32_e32 v26, v26
	v_cvt_f32_i32_e32 v23, v23
	v_cvt_f32_i32_e32 v22, v22
	v_cvt_f32_i32_e32 v19, v19
	v_cvt_f32_i32_e32 v18, v18
	v_cvt_f32_i32_e32 v33, v33
	v_cvt_f32_i32_e32 v32, v32
	v_cvt_f32_i32_e32 v29, v29
	v_cvt_f32_i32_e32 v28, v28
	v_cvt_f32_i32_e32 v25, v25
	v_cvt_f32_i32_e32 v24, v24
	v_cvt_f32_i32_e32 v21, v21
	v_cvt_f32_i32_e32 v20, v20
	v_cvt_f32_i32_e32 v15, v15
	v_cvt_f32_i32_e32 v14, v14
	v_cvt_f32_i32_e32 v11, v11
	v_cvt_f32_i32_e32 v10, v10
	v_cvt_f32_i32_e32 v127, v127
	v_cvt_f32_i32_e32 v126, v126
	v_cvt_f32_i32_e32 v123, v123
	v_cvt_f32_i32_e32 v122, v122
	v_cvt_f32_i32_e32 v111, v111
	v_cvt_f32_i32_e32 v110, v110
	v_cvt_f32_i32_e32 v107, v107
	v_cvt_f32_i32_e32 v106, v106
	v_cvt_f32_i32_e32 v95, v95
	v_cvt_f32_i32_e32 v94, v94
	v_cvt_f32_i32_e32 v91, v91
	v_cvt_f32_i32_e32 v90, v90
	v_cvt_f32_i32_e32 v79, v79
	v_cvt_f32_i32_e32 v78, v78
	v_cvt_f32_i32_e32 v75, v75
	v_cvt_f32_i32_e32 v74, v74
	v_cvt_f32_i32_e32 v17, v17
	v_cvt_f32_i32_e32 v16, v16
	v_cvt_f32_i32_e32 v13, v13
	v_cvt_f32_i32_e32 v12, v12
	v_cvt_f32_i32_e32 v7, v7
	v_cvt_f32_i32_e32 v6, v6
	v_cvt_f32_i32_e32 v3, v3
	v_cvt_f32_i32_e32 v2, v2
	v_cvt_f32_i32_e32 v129, v129
	v_cvt_f32_i32_e32 v128, v128
	v_cvt_f32_i32_e32 v125, v125
	v_cvt_f32_i32_e32 v124, v124
	v_cvt_f32_i32_e32 v113, v113
	v_cvt_f32_i32_e32 v112, v112
	v_cvt_f32_i32_e32 v109, v109
	v_cvt_f32_i32_e32 v108, v108
	v_cvt_f32_i32_e32 v97, v97
	v_cvt_f32_i32_e32 v96, v96
	v_cvt_f32_i32_e32 v93, v93
	v_cvt_f32_i32_e32 v92, v92
	v_cvt_f32_i32_e32 v81, v81
	v_cvt_f32_i32_e32 v80, v80
	v_cvt_f32_i32_e32 v77, v77
	v_cvt_f32_i32_e32 v76, v76
	v_cvt_f32_i32_e32 v9, v9
	v_cvt_f32_i32_e32 v8, v8
	v_cvt_f32_i32_e32 v5, v5
	v_cvt_f32_i32_e32 v4, v4
	s_waitcnt vmcnt(0)
	v_pk_mul_f32 v[158:159], v[142:143], s[66:67] op_sel_hi:[1,0]
	v_pk_mul_f32 v[142:143], v[138:139], s[66:67] op_sel_hi:[1,0]
	v_pk_mul_f32 v[138:139], v[134:135], s[66:67] op_sel_hi:[1,0]
	v_pk_mul_f32 v[130:131], v[130:131], s[66:67] op_sel_hi:[1,0]
	v_mul_f32_e32 v180, 0xbab8aa3b, v160
	v_pk_fma_f32 v[118:119], v[180:181], v[118:119], v[138:139] op_sel_hi:[0,1,1]
	v_pk_fma_f32 v[114:115], v[180:181], v[114:115], v[130:131] op_sel_hi:[0,1,1]
	v_pk_mul_f32 v[136:137], v[136:137], s[66:67] op_sel_hi:[1,0]
	v_pk_mul_f32 v[132:133], v[132:133], s[66:67] op_sel_hi:[1,0]
	v_exp_f32_e32 v118, v118
	v_exp_f32_e32 v114, v114
	v_exp_f32_e32 v119, v119
	v_exp_f32_e32 v115, v115


	v_pk_fma_f32 v[120:121], v[180:181], v[120:121], v[136:137] op_sel_hi:[0,1,1]
	v_pk_fma_f32 v[116:117], v[180:181], v[116:117], v[132:133] op_sel_hi:[0,1,1]
	v_exp_f32_e32 v120, v120
	v_exp_f32_e32 v116, v116
	v_exp_f32_e32 v121, v121
	v_exp_f32_e32 v117, v117


	v_mul_f32_e32 v174, 0xbab8aa3b, v162
	v_pk_fma_f32 v[118:119], v[118:119], s[64:65], s[64:65] op_sel_hi:[1,0,0]
	v_pk_fma_f32 v[114:115], v[114:115], s[64:65], s[64:65] op_sel_hi:[1,0,0]
	v_pk_fma_f32 v[102:103], v[174:175], v[102:103], v[138:139] op_sel_hi:[0,1,1]
	v_pk_fma_f32 v[98:99], v[174:175], v[98:99], v[130:131] op_sel_hi:[0,1,1]
	v_rcp_f32_e32 v118, v118
	v_rcp_f32_e32 v114, v114
	v_exp_f32_e32 v102, v102
	v_exp_f32_e32 v98, v98
	v_exp_f32_e32 v103, v103
	v_exp_f32_e32 v99, v99


	v_pk_fma_f32 v[120:121], v[120:121], s[64:65], s[64:65] op_sel_hi:[1,0,0]
	v_pk_fma_f32 v[116:117], v[116:117], s[64:65], s[64:65] op_sel_hi:[1,0,0]
	v_rcp_f32_e32 v119, v119
	v_rcp_f32_e32 v115, v115
	v_pk_fma_f32 v[104:105], v[174:175], v[104:105], v[136:137] op_sel_hi:[0,1,1]
	v_pk_fma_f32 v[100:101], v[174:175], v[100:101], v[132:133] op_sel_hi:[0,1,1]
	v_rcp_f32_e32 v120, v120
	v_rcp_f32_e32 v116, v116
	v_exp_f32_e32 v104, v104
	v_exp_f32_e32 v100, v100
	v_exp_f32_e32 v105, v105
	v_exp_f32_e32 v101, v101


	v_mul_f32_e32 v172, 0xbab8aa3b, v164
	v_rcp_f32_e32 v121, v121
	v_rcp_f32_e32 v117, v117
	v_rndne_f32_e32 v118, v118
	v_rndne_f32_e32 v114, v114
	v_pk_fma_f32 v[102:103], v[102:103], s[64:65], s[64:65] op_sel_hi:[1,0,0]
	v_pk_fma_f32 v[98:99], v[98:99], s[64:65], s[64:65] op_sel_hi:[1,0,0]
	v_pk_fma_f32 v[86:87], v[172:173], v[86:87], v[138:139] op_sel_hi:[0,1,1]
	v_pk_fma_f32 v[82:83], v[172:173], v[82:83], v[130:131] op_sel_hi:[0,1,1]
	v_cvt_pk_u8_f32 v118, v118, 0, 0
	v_cvt_pk_u8_f32 v114, v114, 0, 0
	v_rndne_f32_e32 v119, v119
	v_rndne_f32_e32 v115, v115
	v_rcp_f32_e32 v102, v102
	v_rcp_f32_e32 v98, v98
	v_exp_f32_e32 v86, v86
	v_exp_f32_e32 v82, v82
	v_exp_f32_e32 v87, v87
	v_exp_f32_e32 v83, v83


	v_cvt_pk_u8_f32 v118, v119, 1, v118
	v_cvt_pk_u8_f32 v114, v115, 1, v114
	v_rndne_f32_e32 v115, v120
	v_rndne_f32_e32 v116, v116
	v_pk_fma_f32 v[104:105], v[104:105], s[64:65], s[64:65] op_sel_hi:[1,0,0]
	v_pk_fma_f32 v[100:101], v[100:101], s[64:65], s[64:65] op_sel_hi:[1,0,0]
	v_rcp_f32_e32 v103, v103
	v_rcp_f32_e32 v99, v99
	v_pk_fma_f32 v[88:89], v[172:173], v[88:89], v[136:137] op_sel_hi:[0,1,1]
	v_pk_fma_f32 v[84:85], v[172:173], v[84:85], v[132:133] op_sel_hi:[0,1,1]
	v_lshlrev_b64 v[178:179], 12, v[170:171]
	v_cvt_pk_u8_f32 v115, v115, 2, v118
	v_cvt_pk_u8_f32 v116, v116, 2, v114
	v_rndne_f32_e32 v114, v121
	v_rcp_f32_e32 v104, v104
	v_rcp_f32_e32 v100, v100
	v_exp_f32_e32 v88, v88
	v_exp_f32_e32 v84, v84
	v_exp_f32_e32 v89, v89
	v_exp_f32_e32 v85, v85


	v_pk_mul_f32 v[156:157], v[144:145], s[66:67] op_sel_hi:[1,0]
	v_pk_mul_f32 v[144:145], v[140:141], s[66:67] op_sel_hi:[1,0]
	v_mul_f32_e32 v166, 0xbab8aa3b, v165
	v_lshl_add_u64 v[140:141], s[10:11], 0, v[178:179]
	v_cvt_pk_u8_f32 v114, v114, 3, v115
	v_rndne_f32_e32 v115, v117
	v_rcp_f32_e32 v105, v105
	v_lshl_add_u64 v[140:141], v[140:141], 0, v[168:169]
	v_cvt_pk_u8_f32 v115, v115, 3, v116
	v_rcp_f32_e32 v101, v101
	v_rndne_f32_e32 v102, v102
	v_rndne_f32_e32 v98, v98
	v_pk_fma_f32 v[86:87], v[86:87], s[64:65], s[64:65] op_sel_hi:[1,0,0]
	v_pk_fma_f32 v[82:83], v[82:83], s[64:65], s[64:65] op_sel_hi:[1,0,0]
	v_pk_fma_f32 v[70:71], v[166:167], v[70:71], v[138:139] op_sel_hi:[0,1,1]
	v_pk_fma_f32 v[66:67], v[166:167], v[66:67], v[130:131] op_sel_hi:[0,1,1]


	v_mul_f32_e32 v164, 0xbab8aa3b, v167
	global_store_dwordx2 v[140:141], v[114:115], off offset:128
	v_or_b32_e32 v114, 16, v170
	v_cvt_pk_u8_f32 v102, v102, 0, 0
	v_cvt_pk_u8_f32 v98, v98, 0, 0
	v_rndne_f32_e32 v103, v103
	v_rndne_f32_e32 v99, v99
	v_rcp_f32_e32 v86, v86
	v_rcp_f32_e32 v82, v82
	v_exp_f32_e32 v70, v70
	v_exp_f32_e32 v66, v66
	v_exp_f32_e32 v71, v71
	v_exp_f32_e32 v67, v67
	v_ashrrev_i32_e32 v115, 31, v114
	v_cvt_pk_u8_f32 v102, v103, 1, v102
	v_cvt_pk_u8_f32 v98, v99, 1, v98
	v_rndne_f32_e32 v99, v104
	v_rndne_f32_e32 v100, v100
	v_pk_fma_f32 v[88:89], v[88:89], s[64:65], s[64:65] op_sel_hi:[1,0,0]
	v_pk_fma_f32 v[84:85], v[84:85], s[64:65], s[64:65] op_sel_hi:[1,0,0]
	v_rcp_f32_e32 v87, v87
	v_rcp_f32_e32 v83, v83
	v_pk_fma_f32 v[72:73], v[166:167], v[72:73], v[136:137] op_sel_hi:[0,1,1]
	v_pk_fma_f32 v[68:69], v[166:167], v[68:69], v[132:133] op_sel_hi:[0,1,1]
	v_pk_fma_f32 v[62:63], v[164:165], v[62:63], v[158:159] op_sel_hi:[0,1,1]
	v_pk_fma_f32 v[58:59], v[164:165], v[58:59], v[142:143] op_sel_hi:[0,1,1]
	v_pk_fma_f32 v[54:55], v[164:165], v[54:55], v[138:139] op_sel_hi:[0,1,1]
	v_pk_fma_f32 v[50:51], v[164:165], v[50:51], v[130:131] op_sel_hi:[0,1,1]


	v_mul_f32_e32 v162, 0xbab8aa3b, v173
	v_lshlrev_b64 v[114:115], 12, v[114:115]
	v_cvt_pk_u8_f32 v99, v99, 2, v102
	v_cvt_pk_u8_f32 v100, v100, 2, v98
	v_rndne_f32_e32 v98, v105
	v_rcp_f32_e32 v88, v88
	v_rcp_f32_e32 v84, v84
	v_exp_f32_e32 v72, v72
	v_exp_f32_e32 v68, v68
	v_exp_f32_e32 v73, v73
	v_exp_f32_e32 v69, v69
	v_exp_f32_e32 v62, v62
	v_exp_f32_e32 v58, v58
	v_exp_f32_e32 v63, v63
	v_exp_f32_e32 v59, v59
	v_exp_f32_e32 v54, v54
	v_exp_f32_e32 v50, v50
	v_exp_f32_e32 v55, v55
	v_exp_f32_e32 v51, v51
	v_lshl_add_u64 v[114:115], s[10:11], 0, v[114:115]
	v_cvt_pk_u8_f32 v98, v98, 3, v99
	v_rndne_f32_e32 v99, v101
	v_rcp_f32_e32 v89, v89
	v_pk_fma_f32 v[64:65], v[164:165], v[64:65], v[156:157] op_sel_hi:[0,1,1]
	v_pk_fma_f32 v[60:61], v[164:165], v[60:61], v[144:145] op_sel_hi:[0,1,1]
	v_pk_fma_f32 v[56:57], v[164:165], v[56:57], v[136:137] op_sel_hi:[0,1,1]
	v_pk_fma_f32 v[52:53], v[164:165], v[52:53], v[132:133] op_sel_hi:[0,1,1]
	v_pk_fma_f32 v[46:47], v[162:163], v[46:47], v[158:159] op_sel_hi:[0,1,1]
	v_pk_fma_f32 v[42:43], v[162:163], v[42:43], v[142:143] op_sel_hi:[0,1,1]
	v_pk_fma_f32 v[38:39], v[162:163], v[38:39], v[138:139] op_sel_hi:[0,1,1]
	v_pk_fma_f32 v[34:35], v[162:163], v[34:35], v[130:131] op_sel_hi:[0,1,1]


	v_mul_f32_e32 v160, 0xbab8aa3b, v175
	v_lshl_add_u64 v[114:115], v[114:115], 0, v[168:169]
	v_cvt_pk_u8_f32 v99, v99, 3, v100
	v_rcp_f32_e32 v85, v85
	v_rndne_f32_e32 v86, v86
	v_rndne_f32_e32 v82, v82
	v_pk_fma_f32 v[70:71], v[70:71], s[64:65], s[64:65] op_sel_hi:[1,0,0]
	v_pk_fma_f32 v[66:67], v[66:67], s[64:65], s[64:65] op_sel_hi:[1,0,0]
	v_exp_f32_e32 v64, v64
	v_exp_f32_e32 v60, v60
	v_exp_f32_e32 v65, v65
	v_exp_f32_e32 v61, v61
	v_exp_f32_e32 v56, v56
	v_exp_f32_e32 v52, v52
	v_exp_f32_e32 v57, v57
	v_exp_f32_e32 v53, v53
	v_exp_f32_e32 v46, v46
	v_exp_f32_e32 v42, v42
	v_exp_f32_e32 v47, v47
	v_exp_f32_e32 v43, v43
	v_exp_f32_e32 v38, v38
	v_exp_f32_e32 v34, v34
	v_exp_f32_e32 v39, v39
	v_exp_f32_e32 v35, v35


	global_store_dwordx2 v[114:115], v[98:99], off offset:128
	v_or_b32_e32 v98, 32, v170


	v_cvt_pk_u8_f32 v86, v86, 0, 0
	v_cvt_pk_u8_f32 v82, v82, 0, 0
	v_rndne_f32_e32 v87, v87
	v_rndne_f32_e32 v83, v83


	v_rcp_f32_e32 v70, v70
	v_rcp_f32_e32 v66, v66
	v_pk_fma_f32 v[48:49], v[162:163], v[48:49], v[156:157] op_sel_hi:[0,1,1]
	v_pk_fma_f32 v[44:45], v[162:163], v[44:45], v[144:145] op_sel_hi:[0,1,1]
	v_pk_fma_f32 v[40:41], v[162:163], v[40:41], v[136:137] op_sel_hi:[0,1,1]
	v_pk_fma_f32 v[36:37], v[162:163], v[36:37], v[132:133] op_sel_hi:[0,1,1]
	v_pk_fma_f32 v[30:31], v[160:161], v[30:31], v[158:159] op_sel_hi:[0,1,1]
	v_pk_fma_f32 v[26:27], v[160:161], v[26:27], v[142:143] op_sel_hi:[0,1,1]
	v_pk_fma_f32 v[22:23], v[160:161], v[22:23], v[138:139] op_sel_hi:[0,1,1]
	v_pk_fma_f32 v[18:19], v[160:161], v[18:19], v[130:131] op_sel_hi:[0,1,1]


	v_mul_f32_e32 v134, 0xbab8aa3b, v176
	v_ashrrev_i32_e32 v99, 31, v98
	v_cvt_pk_u8_f32 v86, v87, 1, v86
	v_cvt_pk_u8_f32 v82, v83, 1, v82
	v_rndne_f32_e32 v83, v88
	v_rndne_f32_e32 v84, v84
	v_pk_fma_f32 v[72:73], v[72:73], s[64:65], s[64:65] op_sel_hi:[1,0,0]
	v_pk_fma_f32 v[68:69], v[68:69], s[64:65], s[64:65] op_sel_hi:[1,0,0]
	v_rcp_f32_e32 v71, v71
	v_rcp_f32_e32 v67, v67
	v_pk_fma_f32 v[62:63], v[62:63], s[64:65], s[64:65] op_sel_hi:[1,0,0]
	v_pk_fma_f32 v[58:59], v[58:59], s[64:65], s[64:65] op_sel_hi:[1,0,0]
	v_pk_fma_f32 v[54:55], v[54:55], s[64:65], s[64:65] op_sel_hi:[1,0,0]
	v_pk_fma_f32 v[50:51], v[50:51], s[64:65], s[64:65] op_sel_hi:[1,0,0]
	v_exp_f32_e32 v48, v48
	v_exp_f32_e32 v44, v44
	v_exp_f32_e32 v49, v49
	v_exp_f32_e32 v45, v45
	v_exp_f32_e32 v40, v40
	v_exp_f32_e32 v36, v36
	v_exp_f32_e32 v41, v41
	v_exp_f32_e32 v37, v37
	v_exp_f32_e32 v30, v30
	v_exp_f32_e32 v26, v26
	v_exp_f32_e32 v31, v31
	v_exp_f32_e32 v27, v27
	v_exp_f32_e32 v22, v22
	v_exp_f32_e32 v18, v18
	v_exp_f32_e32 v23, v23
	v_exp_f32_e32 v19, v19


	v_lshlrev_b64 v[98:99], 12, v[98:99]


	v_cvt_pk_u8_f32 v83, v83, 2, v86
	v_cvt_pk_u8_f32 v84, v84, 2, v82
	v_rndne_f32_e32 v82, v89


	v_rcp_f32_e32 v72, v72
	v_rcp_f32_e32 v68, v68
	v_rcp_f32_e32 v62, v62
	v_rcp_f32_e32 v58, v58
	v_rcp_f32_e32 v54, v54
	v_rcp_f32_e32 v50, v50
	v_pk_fma_f32 v[32:33], v[160:161], v[32:33], v[156:157] op_sel_hi:[0,1,1]
	v_pk_fma_f32 v[28:29], v[160:161], v[28:29], v[144:145] op_sel_hi:[0,1,1]
	v_pk_fma_f32 v[24:25], v[160:161], v[24:25], v[136:137] op_sel_hi:[0,1,1]
	v_pk_fma_f32 v[20:21], v[160:161], v[20:21], v[132:133] op_sel_hi:[0,1,1]
	v_pk_fma_f32 v[14:15], v[134:135], v[14:15], v[158:159] op_sel_hi:[0,1,1]
	v_pk_fma_f32 v[10:11], v[134:135], v[10:11], v[142:143] op_sel_hi:[0,1,1]


	v_lshl_add_u64 v[98:99], s[10:11], 0, v[98:99]
	v_cvt_pk_u8_f32 v82, v82, 3, v83
	v_rndne_f32_e32 v83, v85
	v_rcp_f32_e32 v73, v73
	v_pk_fma_f32 v[64:65], v[64:65], s[64:65], s[64:65] op_sel_hi:[1,0,0]
	v_pk_fma_f32 v[60:61], v[60:61], s[64:65], s[64:65] op_sel_hi:[1,0,0]
	v_rcp_f32_e32 v63, v63
	v_rcp_f32_e32 v59, v59
	v_pk_fma_f32 v[56:57], v[56:57], s[64:65], s[64:65] op_sel_hi:[1,0,0]
	v_pk_fma_f32 v[52:53], v[52:53], s[64:65], s[64:65] op_sel_hi:[1,0,0]
	v_rcp_f32_e32 v55, v55
	v_rcp_f32_e32 v51, v51
	v_pk_fma_f32 v[46:47], v[46:47], s[64:65], s[64:65] op_sel_hi:[1,0,0]
	v_pk_fma_f32 v[42:43], v[42:43], s[64:65], s[64:65] op_sel_hi:[1,0,0]
	v_pk_fma_f32 v[38:39], v[38:39], s[64:65], s[64:65] op_sel_hi:[1,0,0]
	v_pk_fma_f32 v[34:35], v[34:35], s[64:65], s[64:65] op_sel_hi:[1,0,0]
	v_exp_f32_e32 v32, v32
	v_exp_f32_e32 v28, v28
	v_exp_f32_e32 v33, v33
	v_exp_f32_e32 v29, v29
	v_exp_f32_e32 v24, v24
	v_exp_f32_e32 v20, v20
	v_exp_f32_e32 v25, v25
	v_exp_f32_e32 v21, v21
	v_exp_f32_e32 v14, v14
	v_exp_f32_e32 v10, v10
	v_exp_f32_e32 v15, v15
	v_exp_f32_e32 v11, v11
	v_pk_fma_f32 v[126:127], v[180:181], v[126:127], v[158:159] op_sel_hi:[0,1,1]
	v_pk_fma_f32 v[122:123], v[180:181], v[122:123], v[142:143] op_sel_hi:[0,1,1]
	v_pk_fma_f32 v[110:111], v[174:175], v[110:111], v[158:159] op_sel_hi:[0,1,1]
	v_pk_fma_f32 v[106:107], v[174:175], v[106:107], v[142:143] op_sel_hi:[0,1,1]
	v_lshl_add_u64 v[98:99], v[98:99], 0, v[168:169]
	v_pk_fma_f32 v[94:95], v[172:173], v[94:95], v[158:159] op_sel_hi:[0,1,1]
	v_pk_fma_f32 v[90:91], v[172:173], v[90:91], v[142:143] op_sel_hi:[0,1,1]
	v_cvt_pk_u8_f32 v83, v83, 3, v84
	v_pk_fma_f32 v[78:79], v[166:167], v[78:79], v[158:159] op_sel_hi:[0,1,1]
	v_pk_fma_f32 v[74:75], v[166:167], v[74:75], v[142:143] op_sel_hi:[0,1,1]
	v_rcp_f32_e32 v69, v69
	v_rndne_f32_e32 v70, v70
	v_rndne_f32_e32 v66, v66
	v_rcp_f32_e32 v64, v64
	v_rcp_f32_e32 v60, v60
	v_rcp_f32_e32 v56, v56
	v_rcp_f32_e32 v52, v52
	v_rcp_f32_e32 v46, v46
	v_rcp_f32_e32 v42, v42
	v_rcp_f32_e32 v38, v38
	v_rcp_f32_e32 v34, v34
	v_pk_fma_f32 v[16:17], v[134:135], v[16:17], v[156:157] op_sel_hi:[0,1,1]
	v_pk_fma_f32 v[12:13], v[134:135], v[12:13], v[144:145] op_sel_hi:[0,1,1]
	v_pk_fma_f32 v[6:7], v[134:135], v[6:7], v[138:139] op_sel_hi:[0,1,1]
	v_pk_fma_f32 v[2:3], v[134:135], v[2:3], v[130:131] op_sel_hi:[0,1,1]
	v_exp_f32_e32 v126, v126
	v_exp_f32_e32 v122, v122
	v_exp_f32_e32 v127, v127
	v_exp_f32_e32 v123, v123
	v_exp_f32_e32 v110, v110
	v_exp_f32_e32 v106, v106
	v_exp_f32_e32 v111, v111
	v_exp_f32_e32 v107, v107
	v_exp_f32_e32 v94, v94
	v_exp_f32_e32 v90, v90
	v_exp_f32_e32 v95, v95
	v_exp_f32_e32 v91, v91
	global_store_dwordx2 v[98:99], v[82:83], off offset:128
	v_or_b32_e32 v82, 48, v170
	v_exp_f32_e32 v78, v78
	v_exp_f32_e32 v74, v74
	v_exp_f32_e32 v79, v79
	v_exp_f32_e32 v75, v75
	v_cvt_pk_u8_f32 v70, v70, 0, 0
	v_cvt_pk_u8_f32 v66, v66, 0, 0
	v_rndne_f32_e32 v71, v71
	v_rndne_f32_e32 v67, v67
	v_rcp_f32_e32 v65, v65
	v_rcp_f32_e32 v57, v57
	v_pk_fma_f32 v[48:49], v[48:49], s[64:65], s[64:65] op_sel_hi:[1,0,0]
	v_pk_fma_f32 v[44:45], v[44:45], s[64:65], s[64:65] op_sel_hi:[1,0,0]
	v_rcp_f32_e32 v47, v47
	v_rcp_f32_e32 v43, v43
	v_pk_fma_f32 v[40:41], v[40:41], s[64:65], s[64:65] op_sel_hi:[1,0,0]
	v_pk_fma_f32 v[36:37], v[36:37], s[64:65], s[64:65] op_sel_hi:[1,0,0]
	v_rcp_f32_e32 v39, v39
	v_rcp_f32_e32 v35, v35
	v_pk_fma_f32 v[30:31], v[30:31], s[64:65], s[64:65] op_sel_hi:[1,0,0]
	v_pk_fma_f32 v[26:27], v[26:27], s[64:65], s[64:65] op_sel_hi:[1,0,0]
	v_pk_fma_f32 v[22:23], v[22:23], s[64:65], s[64:65] op_sel_hi:[1,0,0]
	v_pk_fma_f32 v[18:19], v[18:19], s[64:65], s[64:65] op_sel_hi:[1,0,0]
	v_exp_f32_e32 v16, v16
	v_exp_f32_e32 v12, v12
	v_exp_f32_e32 v17, v17
	v_exp_f32_e32 v13, v13
	v_exp_f32_e32 v6, v6
	v_exp_f32_e32 v2, v2
	v_exp_f32_e32 v7, v7
	v_exp_f32_e32 v3, v3
	v_pk_fma_f32 v[128:129], v[180:181], v[128:129], v[156:157] op_sel_hi:[0,1,1]
	v_pk_fma_f32 v[124:125], v[180:181], v[124:125], v[144:145] op_sel_hi:[0,1,1]
	v_pk_fma_f32 v[112:113], v[174:175], v[112:113], v[156:157] op_sel_hi:[0,1,1]
	v_pk_fma_f32 v[108:109], v[174:175], v[108:109], v[144:145] op_sel_hi:[0,1,1]
	v_pk_fma_f32 v[96:97], v[172:173], v[96:97], v[156:157] op_sel_hi:[0,1,1]
	v_pk_fma_f32 v[92:93], v[172:173], v[92:93], v[144:145] op_sel_hi:[0,1,1]
	v_ashrrev_i32_e32 v83, 31, v82
	v_pk_fma_f32 v[80:81], v[166:167], v[80:81], v[156:157] op_sel_hi:[0,1,1]
	v_pk_fma_f32 v[76:77], v[166:167], v[76:77], v[144:145] op_sel_hi:[0,1,1]
	v_cvt_pk_u8_f32 v70, v71, 1, v70
	v_cvt_pk_u8_f32 v66, v67, 1, v66
	v_rndne_f32_e32 v67, v72
	v_rndne_f32_e32 v68, v68
	v_rcp_f32_e32 v61, v61
	v_rndne_f32_e32 v62, v62
	v_rndne_f32_e32 v58, v58
	v_rcp_f32_e32 v53, v53
	v_rndne_f32_e32 v54, v54
	v_rndne_f32_e32 v50, v50
	v_rcp_f32_e32 v48, v48
	v_rcp_f32_e32 v44, v44
	v_rcp_f32_e32 v40, v40
	v_rcp_f32_e32 v36, v36
	v_rcp_f32_e32 v30, v30
	v_rcp_f32_e32 v26, v26
	v_rcp_f32_e32 v22, v22
	v_rcp_f32_e32 v18, v18
	v_pk_fma_f32 v[8:9], v[134:135], v[8:9], v[136:137] op_sel_hi:[0,1,1]
	v_pk_fma_f32 v[4:5], v[134:135], v[4:5], v[132:133] op_sel_hi:[0,1,1]
	v_exp_f32_e32 v128, v128
	v_exp_f32_e32 v124, v124
	v_exp_f32_e32 v129, v129
	v_exp_f32_e32 v125, v125
	v_exp_f32_e32 v112, v112
	v_exp_f32_e32 v108, v108
	v_exp_f32_e32 v113, v113
	v_exp_f32_e32 v109, v109
	v_exp_f32_e32 v96, v96
	v_exp_f32_e32 v92, v92
	v_exp_f32_e32 v97, v97
	v_exp_f32_e32 v93, v93
	v_lshlrev_b64 v[82:83], 12, v[82:83]
	v_exp_f32_e32 v80, v80
	v_exp_f32_e32 v76, v76
	v_exp_f32_e32 v81, v81
	v_exp_f32_e32 v77, v77
	v_cvt_pk_u8_f32 v67, v67, 2, v70
	v_cvt_pk_u8_f32 v68, v68, 2, v66
	v_rndne_f32_e32 v66, v73
	v_cvt_pk_u8_f32 v62, v62, 0, 0
	v_cvt_pk_u8_f32 v58, v58, 0, 0
	v_rndne_f32_e32 v63, v63
	v_rndne_f32_e32 v59, v59
	v_cvt_pk_u8_f32 v54, v54, 0, 0
	v_cvt_pk_u8_f32 v50, v50, 0, 0
	v_rndne_f32_e32 v55, v55
	v_rndne_f32_e32 v51, v51
	v_rcp_f32_e32 v49, v49
	v_rcp_f32_e32 v41, v41
	v_pk_fma_f32 v[32:33], v[32:33], s[64:65], s[64:65] op_sel_hi:[1,0,0]
	v_pk_fma_f32 v[28:29], v[28:29], s[64:65], s[64:65] op_sel_hi:[1,0,0]
	v_rcp_f32_e32 v31, v31
	v_rcp_f32_e32 v27, v27
	v_pk_fma_f32 v[24:25], v[24:25], s[64:65], s[64:65] op_sel_hi:[1,0,0]
	v_pk_fma_f32 v[20:21], v[20:21], s[64:65], s[64:65] op_sel_hi:[1,0,0]
	v_rcp_f32_e32 v23, v23
	v_rcp_f32_e32 v19, v19
	v_pk_fma_f32 v[14:15], v[14:15], s[64:65], s[64:65] op_sel_hi:[1,0,0]
	v_pk_fma_f32 v[10:11], v[10:11], s[64:65], s[64:65] op_sel_hi:[1,0,0]
	v_exp_f32_e32 v8, v8
	v_exp_f32_e32 v4, v4
	v_exp_f32_e32 v9, v9
	v_exp_f32_e32 v5, v5
	v_lshl_add_u64 v[82:83], s[10:11], 0, v[82:83]
	v_cvt_pk_u8_f32 v66, v66, 3, v67
	v_rndne_f32_e32 v67, v69
	v_cvt_pk_u8_f32 v62, v63, 1, v62
	v_cvt_pk_u8_f32 v58, v59, 1, v58
	v_rndne_f32_e32 v59, v64
	v_rndne_f32_e32 v60, v60
	v_cvt_pk_u8_f32 v54, v55, 1, v54
	v_cvt_pk_u8_f32 v50, v51, 1, v50
	v_rndne_f32_e32 v51, v56
	v_rndne_f32_e32 v52, v52
	v_rcp_f32_e32 v45, v45
	v_rndne_f32_e32 v46, v46
	v_rndne_f32_e32 v42, v42
	v_rcp_f32_e32 v37, v37
	v_rndne_f32_e32 v38, v38
	v_rndne_f32_e32 v34, v34
	v_rcp_f32_e32 v32, v32
	v_rcp_f32_e32 v28, v28
	v_rcp_f32_e32 v24, v24
	v_rcp_f32_e32 v20, v20
	v_rcp_f32_e32 v14, v14
	v_rcp_f32_e32 v10, v10
	v_pk_fma_f32 v[126:127], v[126:127], s[64:65], s[64:65] op_sel_hi:[1,0,0]
	v_pk_fma_f32 v[122:123], v[122:123], s[64:65], s[64:65] op_sel_hi:[1,0,0]
	v_pk_fma_f32 v[110:111], v[110:111], s[64:65], s[64:65] op_sel_hi:[1,0,0]
	v_pk_fma_f32 v[106:107], v[106:107], s[64:65], s[64:65] op_sel_hi:[1,0,0]
	v_pk_fma_f32 v[94:95], v[94:95], s[64:65], s[64:65] op_sel_hi:[1,0,0]
	v_pk_fma_f32 v[90:91], v[90:91], s[64:65], s[64:65] op_sel_hi:[1,0,0]
	v_lshl_add_u64 v[82:83], v[82:83], 0, v[168:169]
	v_pk_fma_f32 v[78:79], v[78:79], s[64:65], s[64:65] op_sel_hi:[1,0,0]
	v_pk_fma_f32 v[74:75], v[74:75], s[64:65], s[64:65] op_sel_hi:[1,0,0]
	v_cvt_pk_u8_f32 v67, v67, 3, v68
	s_mov_b64 s[4:5], 0x80000
	v_cvt_pk_u8_f32 v59, v59, 2, v62
	v_cvt_pk_u8_f32 v60, v60, 2, v58
	v_rndne_f32_e32 v58, v65
	v_cvt_pk_u8_f32 v51, v51, 2, v54
	v_cvt_pk_u8_f32 v52, v52, 2, v50
	v_rndne_f32_e32 v50, v57
	v_cvt_pk_u8_f32 v46, v46, 0, 0
	v_cvt_pk_u8_f32 v42, v42, 0, 0
	v_rndne_f32_e32 v47, v47
	v_rndne_f32_e32 v43, v43
	v_cvt_pk_u8_f32 v38, v38, 0, 0
	v_cvt_pk_u8_f32 v34, v34, 0, 0
	v_rndne_f32_e32 v39, v39
	v_rndne_f32_e32 v35, v35
	v_rcp_f32_e32 v33, v33
	v_rcp_f32_e32 v25, v25
	v_pk_fma_f32 v[16:17], v[16:17], s[64:65], s[64:65] op_sel_hi:[1,0,0]
	v_pk_fma_f32 v[12:13], v[12:13], s[64:65], s[64:65] op_sel_hi:[1,0,0]
	v_rcp_f32_e32 v15, v15
	v_rcp_f32_e32 v11, v11
	v_pk_fma_f32 v[6:7], v[6:7], s[64:65], s[64:65] op_sel_hi:[1,0,0]
	v_pk_fma_f32 v[2:3], v[2:3], s[64:65], s[64:65] op_sel_hi:[1,0,0]
	v_rcp_f32_e32 v126, v126
	v_rcp_f32_e32 v122, v122
	v_rcp_f32_e32 v110, v110
	v_rcp_f32_e32 v106, v106
	v_rcp_f32_e32 v94, v94
	v_rcp_f32_e32 v90, v90
	v_rcp_f32_e32 v78, v78
	v_rcp_f32_e32 v74, v74
	global_store_dwordx2 v[82:83], v[66:67], off offset:128
	v_lshl_add_u64 v[66:67], v[140:141], 0, s[4:5]
	v_cvt_pk_u8_f32 v58, v58, 3, v59
	v_rndne_f32_e32 v59, v61
	s_mov_b32 s4, 0x80000
	v_cvt_pk_u8_f32 v50, v50, 3, v51
	v_rndne_f32_e32 v51, v53
	v_cvt_pk_u8_f32 v46, v47, 1, v46
	v_cvt_pk_u8_f32 v42, v43, 1, v42
	v_rndne_f32_e32 v43, v48
	v_rndne_f32_e32 v44, v44
	v_cvt_pk_u8_f32 v38, v39, 1, v38
	v_cvt_pk_u8_f32 v34, v35, 1, v34
	v_rndne_f32_e32 v35, v40
	v_rndne_f32_e32 v36, v36
	v_rcp_f32_e32 v29, v29
	v_rndne_f32_e32 v30, v30
	v_rndne_f32_e32 v26, v26
	v_rcp_f32_e32 v21, v21
	v_rndne_f32_e32 v22, v22
	v_rndne_f32_e32 v18, v18
	v_rcp_f32_e32 v16, v16
	v_rcp_f32_e32 v12, v12
	v_rcp_f32_e32 v6, v6
	v_rcp_f32_e32 v2, v2
	v_pk_fma_f32 v[128:129], v[128:129], s[64:65], s[64:65] op_sel_hi:[1,0,0]
	v_pk_fma_f32 v[124:125], v[124:125], s[64:65], s[64:65] op_sel_hi:[1,0,0]
	v_rcp_f32_e32 v127, v127
	v_rcp_f32_e32 v123, v123
	v_pk_fma_f32 v[112:113], v[112:113], s[64:65], s[64:65] op_sel_hi:[1,0,0]
	v_pk_fma_f32 v[108:109], v[108:109], s[64:65], s[64:65] op_sel_hi:[1,0,0]
	v_rcp_f32_e32 v111, v111
	v_rcp_f32_e32 v107, v107
	v_pk_fma_f32 v[96:97], v[96:97], s[64:65], s[64:65] op_sel_hi:[1,0,0]
	v_pk_fma_f32 v[92:93], v[92:93], s[64:65], s[64:65] op_sel_hi:[1,0,0]
	v_rcp_f32_e32 v95, v95
	v_rcp_f32_e32 v91, v91
	v_pk_fma_f32 v[80:81], v[80:81], s[64:65], s[64:65] op_sel_hi:[1,0,0]
	v_pk_fma_f32 v[76:77], v[76:77], s[64:65], s[64:65] op_sel_hi:[1,0,0]
	v_rcp_f32_e32 v79, v79
	v_rcp_f32_e32 v75, v75
	v_cvt_pk_u8_f32 v59, v59, 3, v60
	v_add_co_u32_e32 v60, vcc, s4, v140
	v_cvt_pk_u8_f32 v51, v51, 3, v52
	s_mov_b64 s[4:5], 0x90000
	v_cvt_pk_u8_f32 v43, v43, 2, v46
	v_cvt_pk_u8_f32 v44, v44, 2, v42
	v_rndne_f32_e32 v42, v49
	v_cvt_pk_u8_f32 v35, v35, 2, v38
	v_cvt_pk_u8_f32 v36, v36, 2, v34
	v_rndne_f32_e32 v34, v41
	v_cvt_pk_u8_f32 v30, v30, 0, 0
	v_cvt_pk_u8_f32 v26, v26, 0, 0
	v_rndne_f32_e32 v31, v31
	v_rndne_f32_e32 v27, v27
	v_cvt_pk_u8_f32 v22, v22, 0, 0
	v_cvt_pk_u8_f32 v18, v18, 0, 0
	v_rndne_f32_e32 v23, v23
	v_rndne_f32_e32 v19, v19
	v_rcp_f32_e32 v17, v17
	v_pk_fma_f32 v[8:9], v[8:9], s[64:65], s[64:65] op_sel_hi:[1,0,0]
	v_pk_fma_f32 v[4:5], v[4:5], s[64:65], s[64:65] op_sel_hi:[1,0,0]
	v_rcp_f32_e32 v7, v7
	v_rcp_f32_e32 v3, v3
	v_rcp_f32_e32 v128, v128
	v_rcp_f32_e32 v124, v124
	v_rcp_f32_e32 v112, v112
	v_rcp_f32_e32 v108, v108
	v_rcp_f32_e32 v96, v96
	v_rcp_f32_e32 v92, v92
	v_rcp_f32_e32 v80, v80
	v_rcp_f32_e32 v76, v76
	v_addc_co_u32_e32 v61, vcc, 0, v141, vcc
	global_store_dwordx2 v[66:67], v[50:51], off offset:128
	v_lshl_add_u64 v[50:51], v[140:141], 0, s[4:5]
	v_cvt_pk_u8_f32 v42, v42, 3, v43
	v_rndne_f32_e32 v43, v45
	s_mov_b32 s4, 0x90000
	v_cvt_pk_u8_f32 v34, v34, 3, v35
	v_rndne_f32_e32 v35, v37
	v_cvt_pk_u8_f32 v30, v31, 1, v30
	v_cvt_pk_u8_f32 v26, v27, 1, v26
	v_rndne_f32_e32 v27, v32
	v_rndne_f32_e32 v28, v28
	v_cvt_pk_u8_f32 v22, v23, 1, v22
	v_cvt_pk_u8_f32 v18, v19, 1, v18
	v_rndne_f32_e32 v19, v24
	v_rndne_f32_e32 v20, v20
	v_rcp_f32_e32 v13, v13
	v_rndne_f32_e32 v14, v14
	v_rndne_f32_e32 v10, v10
	v_rcp_f32_e32 v8, v8
	v_rcp_f32_e32 v4, v4
	v_rcp_f32_e32 v129, v129
	v_rcp_f32_e32 v113, v113
	v_rcp_f32_e32 v97, v97
	v_rcp_f32_e32 v81, v81
	v_cvt_pk_u8_f32 v43, v43, 3, v44
	v_add_co_u32_e32 v44, vcc, s4, v140
	v_cvt_pk_u8_f32 v35, v35, 3, v36
	s_mov_b64 s[4:5], 0xa0000
	v_cvt_pk_u8_f32 v27, v27, 2, v30
	v_cvt_pk_u8_f32 v28, v28, 2, v26
	v_rndne_f32_e32 v26, v33
	v_cvt_pk_u8_f32 v19, v19, 2, v22
	v_cvt_pk_u8_f32 v20, v20, 2, v18
	v_rndne_f32_e32 v18, v25
	v_cvt_pk_u8_f32 v14, v14, 0, 0
	v_cvt_pk_u8_f32 v10, v10, 0, 0
	v_rndne_f32_e32 v15, v15
	v_rndne_f32_e32 v11, v11
	v_rcp_f32_e32 v9, v9
	v_rcp_f32_e32 v125, v125
	v_rndne_f32_e32 v126, v126
	v_rndne_f32_e32 v122, v122
	v_rcp_f32_e32 v109, v109
	v_rndne_f32_e32 v110, v110
	v_rndne_f32_e32 v106, v106
	v_rcp_f32_e32 v93, v93
	v_rndne_f32_e32 v94, v94
	v_rndne_f32_e32 v90, v90
	v_rcp_f32_e32 v77, v77
	v_rndne_f32_e32 v78, v78
	v_rndne_f32_e32 v74, v74
	v_addc_co_u32_e32 v45, vcc, 0, v141, vcc
	global_store_dwordx2 v[50:51], v[34:35], off offset:128
	v_lshl_add_u64 v[34:35], v[140:141], 0, s[4:5]
	v_cvt_pk_u8_f32 v26, v26, 3, v27
	v_rndne_f32_e32 v27, v29
	s_mov_b32 s4, 0xa0000
	v_cvt_pk_u8_f32 v18, v18, 3, v19
	v_rndne_f32_e32 v19, v21
	v_cvt_pk_u8_f32 v14, v15, 1, v14
	v_cvt_pk_u8_f32 v10, v11, 1, v10
	v_rndne_f32_e32 v11, v16
	v_rndne_f32_e32 v12, v12
	v_rcp_f32_e32 v5, v5
	v_rndne_f32_e32 v6, v6
	v_rndne_f32_e32 v2, v2
	v_cvt_pk_u8_f32 v126, v126, 0, 0
	v_cvt_pk_u8_f32 v122, v122, 0, 0
	v_rndne_f32_e32 v127, v127
	v_rndne_f32_e32 v123, v123
	v_cvt_pk_u8_f32 v110, v110, 0, 0
	v_cvt_pk_u8_f32 v106, v106, 0, 0
	v_rndne_f32_e32 v111, v111
	v_rndne_f32_e32 v107, v107
	v_cvt_pk_u8_f32 v94, v94, 0, 0
	v_cvt_pk_u8_f32 v90, v90, 0, 0
	v_rndne_f32_e32 v95, v95
	v_rndne_f32_e32 v91, v91
	v_cvt_pk_u8_f32 v78, v78, 0, 0
	v_cvt_pk_u8_f32 v74, v74, 0, 0
	v_rndne_f32_e32 v79, v79
	v_rndne_f32_e32 v75, v75
	v_cvt_pk_u8_f32 v27, v27, 3, v28
	v_add_co_u32_e32 v28, vcc, s4, v140
	v_cvt_pk_u8_f32 v19, v19, 3, v20
	s_mov_b64 s[4:5], 0xb0000
	v_cvt_pk_u8_f32 v11, v11, 2, v14
	v_cvt_pk_u8_f32 v12, v12, 2, v10
	v_rndne_f32_e32 v10, v17
	v_cvt_pk_u8_f32 v6, v6, 0, 0
	v_cvt_pk_u8_f32 v2, v2, 0, 0
	v_rndne_f32_e32 v7, v7
	v_rndne_f32_e32 v3, v3
	v_cvt_pk_u8_f32 v126, v127, 1, v126
	v_cvt_pk_u8_f32 v122, v123, 1, v122
	v_rndne_f32_e32 v123, v128
	v_rndne_f32_e32 v124, v124
	v_cvt_pk_u8_f32 v110, v111, 1, v110
	v_cvt_pk_u8_f32 v106, v107, 1, v106
	v_rndne_f32_e32 v107, v112
	v_rndne_f32_e32 v108, v108
	v_cvt_pk_u8_f32 v94, v95, 1, v94
	v_cvt_pk_u8_f32 v90, v91, 1, v90
	v_rndne_f32_e32 v91, v96
	v_rndne_f32_e32 v92, v92
	v_cvt_pk_u8_f32 v78, v79, 1, v78
	v_cvt_pk_u8_f32 v74, v75, 1, v74
	v_rndne_f32_e32 v75, v80
	v_rndne_f32_e32 v76, v76
	v_addc_co_u32_e32 v29, vcc, 0, v141, vcc
	global_store_dwordx2 v[34:35], v[18:19], off offset:128
	v_lshl_add_u64 v[18:19], v[140:141], 0, s[4:5]
	v_cvt_pk_u8_f32 v10, v10, 3, v11
	v_rndne_f32_e32 v11, v13
	s_mov_b32 s4, 0xb0000
	v_cvt_pk_u8_f32 v6, v7, 1, v6
	v_cvt_pk_u8_f32 v2, v3, 1, v2
	v_rndne_f32_e32 v3, v8
	v_rndne_f32_e32 v4, v4
	v_cvt_pk_u8_f32 v123, v123, 2, v126
	v_cvt_pk_u8_f32 v124, v124, 2, v122
	v_rndne_f32_e32 v122, v129
	v_cvt_pk_u8_f32 v107, v107, 2, v110
	v_cvt_pk_u8_f32 v108, v108, 2, v106
	v_rndne_f32_e32 v106, v113
	v_cvt_pk_u8_f32 v91, v91, 2, v94
	v_cvt_pk_u8_f32 v92, v92, 2, v90
	v_rndne_f32_e32 v90, v97
	v_cvt_pk_u8_f32 v75, v75, 2, v78
	v_cvt_pk_u8_f32 v76, v76, 2, v74
	v_rndne_f32_e32 v74, v81
	v_cvt_pk_u8_f32 v11, v11, 3, v12
	v_add_co_u32_e32 v12, vcc, s4, v140
	v_cvt_pk_u8_f32 v3, v3, 2, v6
	v_cvt_pk_u8_f32 v4, v4, 2, v2
	v_rndne_f32_e32 v2, v9
	v_cvt_pk_u8_f32 v122, v122, 3, v123
	v_rndne_f32_e32 v123, v125
	v_cvt_pk_u8_f32 v106, v106, 3, v107
	v_rndne_f32_e32 v107, v109
	v_cvt_pk_u8_f32 v90, v90, 3, v91
	v_rndne_f32_e32 v91, v93
	v_cvt_pk_u8_f32 v74, v74, 3, v75
	v_rndne_f32_e32 v75, v77
	v_addc_co_u32_e32 v13, vcc, 0, v141, vcc
	v_cvt_pk_u8_f32 v2, v2, 3, v3
	v_rndne_f32_e32 v3, v5
	v_cvt_pk_u8_f32 v123, v123, 3, v124
	v_cvt_pk_u8_f32 v107, v107, 3, v108
	v_cvt_pk_u8_f32 v91, v91, 3, v92
	v_cvt_pk_u8_f32 v75, v75, 3, v76
	v_cvt_pk_u8_f32 v3, v3, 3, v4
	s_mov_b64 s[26:27], -1
	s_andn2_b64 vcc, exec, s[6:7]
	global_store_dwordx2 v[140:141], v[122:123], off
	global_store_dwordx2 v[114:115], v[106:107], off
	global_store_dwordx2 v[98:99], v[90:91], off
	global_store_dwordx2 v[82:83], v[74:75], off
	global_store_dwordx2 v[60:61], v[58:59], off
	global_store_dwordx2 v[44:45], v[42:43], off
	global_store_dwordx2 v[28:29], v[26:27], off
	global_store_dwordx2 v[12:13], v[10:11], off
	global_store_dwordx2 v[18:19], v[2:3], off offset:128
	s_cbranch_vccnz .LBB0_187
	s_andn2_b64 vcc, exec, s[8:9]
	s_cbranch_vccnz .LBB0_186
	s_barrier
	s_branch .LBB0_186

.LBB0_1177:
	v_cvt_f32_i32_e32 v123, v123
	v_cvt_f32_i32_e32 v122, v122
	v_cvt_f32_i32_e32 v125, v125
	v_cvt_f32_i32_e32 v124, v124
	v_cvt_f32_i32_e32 v119, v119
	v_cvt_f32_i32_e32 v118, v118
	v_cvt_f32_i32_e32 v121, v121
	v_cvt_f32_i32_e32 v120, v120
	v_cvt_f32_i32_e32 v127, v127
	v_cvt_f32_i32_e32 v126, v126
	v_cvt_f32_i32_e32 v117, v117
	v_cvt_f32_i32_e32 v116, v116
	v_cvt_f32_i32_e32 v115, v115
	v_cvt_f32_i32_e32 v114, v114
	v_cvt_f32_i32_e32 v129, v129
	v_cvt_f32_i32_e32 v128, v128
	v_cvt_f32_i32_e32 v107, v107
	v_cvt_f32_i32_e32 v106, v106
	v_cvt_f32_i32_e32 v109, v109
	v_cvt_f32_i32_e32 v108, v108
	v_cvt_f32_i32_e32 v103, v103
	v_cvt_f32_i32_e32 v102, v102
	v_cvt_f32_i32_e32 v105, v105
	v_cvt_f32_i32_e32 v104, v104
	v_cvt_f32_i32_e32 v111, v111
	v_cvt_f32_i32_e32 v110, v110
	v_cvt_f32_i32_e32 v101, v101
	v_cvt_f32_i32_e32 v100, v100
	v_cvt_f32_i32_e32 v99, v99
	v_cvt_f32_i32_e32 v98, v98
	v_cvt_f32_i32_e32 v113, v113
	v_cvt_f32_i32_e32 v112, v112
	v_cvt_f32_i32_e32 v91, v91
	v_cvt_f32_i32_e32 v90, v90
	v_cvt_f32_i32_e32 v93, v93
	v_cvt_f32_i32_e32 v92, v92
	v_cvt_f32_i32_e32 v87, v87
	v_cvt_f32_i32_e32 v86, v86
	v_cvt_f32_i32_e32 v89, v89
	v_cvt_f32_i32_e32 v88, v88
	v_cvt_f32_i32_e32 v95, v95
	v_cvt_f32_i32_e32 v94, v94
	v_cvt_f32_i32_e32 v85, v85
	v_cvt_f32_i32_e32 v84, v84
	v_cvt_f32_i32_e32 v83, v83
	v_cvt_f32_i32_e32 v82, v82
	v_cvt_f32_i32_e32 v97, v97
	v_cvt_f32_i32_e32 v96, v96
	v_cvt_f32_i32_e32 v75, v75
	v_cvt_f32_i32_e32 v74, v74
	v_cvt_f32_i32_e32 v77, v77
	v_cvt_f32_i32_e32 v76, v76
	v_cvt_f32_i32_e32 v71, v71
	v_cvt_f32_i32_e32 v70, v70
	v_cvt_f32_i32_e32 v73, v73
	v_cvt_f32_i32_e32 v72, v72
	v_cvt_f32_i32_e32 v79, v79
	v_cvt_f32_i32_e32 v78, v78
	v_cvt_f32_i32_e32 v69, v69
	v_cvt_f32_i32_e32 v68, v68
	v_cvt_f32_i32_e32 v67, v67
	v_cvt_f32_i32_e32 v66, v66
	v_cvt_f32_i32_e32 v81, v81
	v_cvt_f32_i32_e32 v80, v80
	v_cvt_f32_i32_e32 v59, v59
	v_cvt_f32_i32_e32 v58, v58
	v_cvt_f32_i32_e32 v61, v61
	v_cvt_f32_i32_e32 v60, v60
	v_cvt_f32_i32_e32 v55, v55
	v_cvt_f32_i32_e32 v54, v54
	v_cvt_f32_i32_e32 v57, v57
	v_cvt_f32_i32_e32 v56, v56
	v_cvt_f32_i32_e32 v63, v63
	v_cvt_f32_i32_e32 v62, v62
	v_cvt_f32_i32_e32 v53, v53
	v_cvt_f32_i32_e32 v52, v52
	v_cvt_f32_i32_e32 v51, v51
	v_cvt_f32_i32_e32 v50, v50
	v_cvt_f32_i32_e32 v65, v65
	v_cvt_f32_i32_e32 v64, v64
	v_cvt_f32_i32_e32 v43, v43
	v_cvt_f32_i32_e32 v42, v42
	v_cvt_f32_i32_e32 v45, v45
	v_cvt_f32_i32_e32 v44, v44
	v_cvt_f32_i32_e32 v39, v39
	v_cvt_f32_i32_e32 v38, v38
	v_cvt_f32_i32_e32 v41, v41
	v_cvt_f32_i32_e32 v40, v40
	v_cvt_f32_i32_e32 v47, v47
	v_cvt_f32_i32_e32 v46, v46
	v_cvt_f32_i32_e32 v37, v37
	v_cvt_f32_i32_e32 v36, v36
	v_cvt_f32_i32_e32 v35, v35
	v_cvt_f32_i32_e32 v34, v34
	v_cvt_f32_i32_e32 v49, v49
	v_cvt_f32_i32_e32 v48, v48
	v_cvt_f32_i32_e32 v27, v27
	v_cvt_f32_i32_e32 v26, v26
	v_cvt_f32_i32_e32 v29, v29
	v_cvt_f32_i32_e32 v28, v28
	v_cvt_f32_i32_e32 v23, v23
	v_cvt_f32_i32_e32 v22, v22
	v_cvt_f32_i32_e32 v25, v25
	v_cvt_f32_i32_e32 v24, v24
	v_cvt_f32_i32_e32 v31, v31
	v_cvt_f32_i32_e32 v30, v30
	v_cvt_f32_i32_e32 v21, v21
	v_cvt_f32_i32_e32 v20, v20
	v_cvt_f32_i32_e32 v19, v19
	v_cvt_f32_i32_e32 v18, v18
	v_cvt_f32_i32_e32 v33, v33
	v_cvt_f32_i32_e32 v32, v32
	v_cvt_f32_i32_e32 v11, v11
	v_cvt_f32_i32_e32 v10, v10
	v_cvt_f32_i32_e32 v13, v13
	v_cvt_f32_i32_e32 v12, v12
	v_cvt_f32_i32_e32 v7, v7
	v_cvt_f32_i32_e32 v6, v6
	v_cvt_f32_i32_e32 v9, v9
	v_cvt_f32_i32_e32 v8, v8
	v_cvt_f32_i32_e32 v15, v15
	v_cvt_f32_i32_e32 v14, v14
	v_cvt_f32_i32_e32 v5, v5
	v_cvt_f32_i32_e32 v4, v4
	v_cvt_f32_i32_e32 v3, v3
	v_cvt_f32_i32_e32 v2, v2
	v_cvt_f32_i32_e32 v17, v17
	v_cvt_f32_i32_e32 v16, v16
	s_waitcnt vmcnt(0)
	v_mul_f32_e32 v158, 0x3a800000, v141
	v_mul_f32_e32 v161, 0x3a800000, v147
	v_mul_f32_e32 v147, 0x3a800000, v150
	v_mul_f32_e32 v150, 0xbfb8aa3b, v158
	v_pk_mul_f32 v[154:155], v[150:151], v[122:123] op_sel_hi:[0,1]
	v_mul_f32_e32 v159, 0x3a800000, v143
	v_mul_f32_e32 v160, 0x3a800000, v146
	v_mul_f32_e32 v146, 0x3a800000, v151
	v_mul_f32_e32 v143, 0x3a800000, v152
	v_pk_mul_f32 v[152:153], v[150:151], v[124:125] op_sel_hi:[0,1]
	v_pk_mul_f32 v[156:157], v[150:151], v[120:121] op_sel_hi:[0,1]
	v_pk_mul_f32 v[150:151], v[150:151], v[118:119] op_sel_hi:[0,1]
	v_exp_f32_e32 v154, v154
	v_exp_f32_e32 v155, v155
	v_exp_f32_e32 v150, v150
	v_exp_f32_e32 v151, v151
	v_exp_f32_e32 v156, v156
	v_exp_f32_e32 v157, v157
	v_pk_add_f32 v[154:155], v[154:155], 1.0 op_sel_hi:[1,0]


	v_exp_f32_e32 v152, v152
	v_exp_f32_e32 v153, v153
	v_pk_add_f32 v[156:157], v[156:157], 1.0 op_sel_hi:[1,0]
	v_pk_add_f32 v[150:151], v[150:151], 1.0 op_sel_hi:[1,0]
	v_rcp_f32_e32 v154, v154
	v_rcp_f32_e32 v155, v155


	v_rcp_f32_e32 v150, v150
	v_rcp_f32_e32 v151, v151
	v_rcp_f32_e32 v156, v156
	v_rcp_f32_e32 v157, v157
	v_mul_f32_e32 v158, v158, v158
	v_pk_add_f32 v[152:153], v[152:153], 1.0 op_sel_hi:[1,0]
	v_pk_mul_f32 v[122:123], v[122:123], v[126:127]
	v_pk_mul_f32 v[126:127], v[158:159], v[154:155] op_sel_hi:[0,1]
	s_mul_hi_i32 s5, s28, 0x92492493


	v_rcp_f32_e32 v152, v152
	v_rcp_f32_e32 v153, v153
	v_pk_mul_f32 v[122:123], v[122:123], v[126:127]
	v_pk_mul_f32 v[114:115], v[118:119], v[114:115]
	v_pk_mul_f32 v[116:117], v[120:121], v[116:117]
	v_pk_mul_f32 v[118:119], v[158:159], v[150:151] op_sel_hi:[0,1]
	v_pk_mul_f32 v[120:121], v[158:159], v[156:157] op_sel_hi:[0,1]
	s_add_i32 s5, s5, s28
	v_pk_mul_f32 v[116:117], v[116:117], v[120:121]
	v_pk_mul_f32 v[114:115], v[114:115], v[118:119]
	v_med3_f32 v119, v122, s61, v237
	v_med3_f32 v120, v123, s61, v237
	v_mov_b32_e32 v118, v1
	s_lshr_b32 s17, s5, 31
	s_lshr_b32 s5, s5, 4
	v_cvt_pk_fp8_f32 v118, v119, v120
	v_med3_f32 v114, v114, s61, v237
	v_med3_f32 v115, v115, s61, v237
	v_mov_b32_e32 v119, v1
	s_add_i32 s5, s5, s17
	v_cvt_pk_fp8_f32 v119, v114, v115
	s_mul_i32 s5, s5, 28
	v_pk_mul_f32 v[124:125], v[124:125], v[128:129]
	v_pk_mul_f32 v[128:129], v[158:159], v[152:153] op_sel_hi:[0,1]
	s_sub_i32 s5, s28, s5
	v_pk_mul_f32 v[124:125], v[124:125], v[128:129]
	v_ashrrev_i32_e32 v140, 1, v140
	s_lshl_b32 s5, s5, 7
	v_med3_f32 v121, v124, s61, v237
	v_med3_f32 v122, v125, s61, v237
	v_med3_f32 v114, v116, s61, v237
	v_med3_f32 v115, v117, s61, v237
	v_and_b32_e32 v140, -8, v140
	s_or_b32 s5, s5, s7
	v_cvt_pk_fp8_f32 v118, v121, v122 op_sel:[0,0,1]
	v_cvt_pk_fp8_f32 v119, v114, v115 op_sel:[0,0,1]
	v_add_u32_e32 v140, s5, v140
	v_mov_b64_e32 v[114:115], s[10:11]
	s_movk_i32 s5, 0xe00


	v_ashrrev_i32_e32 v141, 31, v140
	v_mad_i64_i32 v[116:117], s[26:27], v142, s5, v[114:115]


	v_lshl_add_u64 v[116:117], v[116:117], 0, v[140:141]
	global_store_dwordx2 v[116:117], v[118:119], off
	v_mul_f32_e32 v116, 0xbfb8aa3b, v159
	v_pk_mul_f32 v[120:121], v[116:117], v[106:107] op_sel_hi:[0,1]
	v_pk_mul_f32 v[118:119], v[116:117], v[108:109] op_sel_hi:[0,1]
	v_pk_mul_f32 v[122:123], v[116:117], v[104:105] op_sel_hi:[0,1]
	v_pk_mul_f32 v[116:117], v[116:117], v[102:103] op_sel_hi:[0,1]
	v_exp_f32_e32 v120, v120
	v_exp_f32_e32 v121, v121
	v_exp_f32_e32 v116, v116
	v_exp_f32_e32 v117, v117
	v_exp_f32_e32 v122, v122
	v_exp_f32_e32 v123, v123
	v_pk_add_f32 v[120:121], v[120:121], 1.0 op_sel_hi:[1,0]


	v_exp_f32_e32 v118, v118
	v_exp_f32_e32 v119, v119
	v_pk_add_f32 v[122:123], v[122:123], 1.0 op_sel_hi:[1,0]
	v_pk_add_f32 v[116:117], v[116:117], 1.0 op_sel_hi:[1,0]
	v_rcp_f32_e32 v120, v120
	v_rcp_f32_e32 v121, v121


	v_rcp_f32_e32 v116, v116
	v_rcp_f32_e32 v117, v117
	v_rcp_f32_e32 v122, v122
	v_rcp_f32_e32 v123, v123
	v_or_b32_e32 v125, 16, v142
	v_mul_f32_e32 v124, v159, v159
	v_pk_add_f32 v[118:119], v[118:119], 1.0 op_sel_hi:[1,0]
	v_pk_mul_f32 v[106:107], v[106:107], v[110:111]
	v_pk_mul_f32 v[110:111], v[124:125], v[120:121] op_sel_hi:[0,1]


	v_rcp_f32_e32 v118, v118
	v_rcp_f32_e32 v119, v119
	v_pk_mul_f32 v[106:107], v[106:107], v[110:111]
	v_pk_mul_f32 v[98:99], v[102:103], v[98:99]
	v_pk_mul_f32 v[100:101], v[104:105], v[100:101]
	v_pk_mul_f32 v[102:103], v[124:125], v[116:117] op_sel_hi:[0,1]
	v_pk_mul_f32 v[104:105], v[124:125], v[122:123] op_sel_hi:[0,1]
	v_pk_mul_f32 v[100:101], v[100:101], v[104:105]
	v_pk_mul_f32 v[98:99], v[98:99], v[102:103]
	v_med3_f32 v103, v106, s61, v237
	v_med3_f32 v104, v107, s61, v237
	v_mov_b32_e32 v102, v1
	v_cvt_pk_fp8_f32 v102, v103, v104
	v_med3_f32 v98, v98, s61, v237
	v_med3_f32 v99, v99, s61, v237
	v_mov_b32_e32 v103, v1
	v_cvt_pk_fp8_f32 v103, v98, v99
	v_pk_mul_f32 v[108:109], v[108:109], v[112:113]
	v_pk_mul_f32 v[112:113], v[124:125], v[118:119] op_sel_hi:[0,1]
	v_pk_mul_f32 v[108:109], v[108:109], v[112:113]
	v_med3_f32 v98, v100, s61, v237
	v_med3_f32 v105, v108, s61, v237
	v_med3_f32 v106, v109, s61, v237
	v_med3_f32 v99, v101, s61, v237
	v_cvt_pk_fp8_f32 v102, v105, v106 op_sel:[0,0,1]
	v_cvt_pk_fp8_f32 v103, v98, v99 op_sel:[0,0,1]


	v_mad_i64_i32 v[98:99], s[26:27], v125, s5, v[114:115]


	v_lshl_add_u64 v[98:99], v[98:99], 0, v[140:141]
	global_store_dwordx2 v[98:99], v[102:103], off
	v_mul_f32_e32 v98, 0xbfb8aa3b, v160
	v_pk_mul_f32 v[102:103], v[98:99], v[90:91] op_sel_hi:[0,1]
	v_pk_mul_f32 v[100:101], v[98:99], v[92:93] op_sel_hi:[0,1]
	v_pk_mul_f32 v[104:105], v[98:99], v[88:89] op_sel_hi:[0,1]
	v_pk_mul_f32 v[98:99], v[98:99], v[86:87] op_sel_hi:[0,1]
	v_exp_f32_e32 v102, v102
	v_exp_f32_e32 v103, v103
	v_exp_f32_e32 v98, v98
	v_exp_f32_e32 v99, v99
	v_exp_f32_e32 v104, v104
	v_exp_f32_e32 v105, v105
	v_pk_add_f32 v[102:103], v[102:103], 1.0 op_sel_hi:[1,0]


	v_exp_f32_e32 v100, v100
	v_exp_f32_e32 v101, v101
	v_pk_add_f32 v[104:105], v[104:105], 1.0 op_sel_hi:[1,0]
	v_pk_add_f32 v[98:99], v[98:99], 1.0 op_sel_hi:[1,0]
	v_rcp_f32_e32 v102, v102
	v_rcp_f32_e32 v103, v103


	v_rcp_f32_e32 v98, v98
	v_rcp_f32_e32 v99, v99
	v_rcp_f32_e32 v104, v104
	v_rcp_f32_e32 v105, v105
	v_or_b32_e32 v107, 32, v142
	v_mul_f32_e32 v106, v160, v160
	v_pk_add_f32 v[100:101], v[100:101], 1.0 op_sel_hi:[1,0]
	v_pk_mul_f32 v[90:91], v[90:91], v[94:95]
	v_pk_mul_f32 v[94:95], v[106:107], v[102:103] op_sel_hi:[0,1]


	v_rcp_f32_e32 v100, v100
	v_rcp_f32_e32 v101, v101
	v_pk_mul_f32 v[90:91], v[90:91], v[94:95]
	v_pk_mul_f32 v[82:83], v[86:87], v[82:83]
	v_pk_mul_f32 v[84:85], v[88:89], v[84:85]
	v_pk_mul_f32 v[86:87], v[106:107], v[98:99] op_sel_hi:[0,1]
	v_pk_mul_f32 v[88:89], v[106:107], v[104:105] op_sel_hi:[0,1]
	v_pk_mul_f32 v[84:85], v[84:85], v[88:89]
	v_pk_mul_f32 v[82:83], v[82:83], v[86:87]
	v_med3_f32 v87, v90, s61, v237
	v_med3_f32 v88, v91, s61, v237
	v_mov_b32_e32 v86, v1
	v_cvt_pk_fp8_f32 v86, v87, v88
	v_med3_f32 v82, v82, s61, v237
	v_med3_f32 v83, v83, s61, v237
	v_mov_b32_e32 v87, v1
	v_cvt_pk_fp8_f32 v87, v82, v83
	v_pk_mul_f32 v[92:93], v[92:93], v[96:97]
	v_pk_mul_f32 v[96:97], v[106:107], v[100:101] op_sel_hi:[0,1]
	v_pk_mul_f32 v[92:93], v[92:93], v[96:97]
	v_med3_f32 v82, v84, s61, v237
	v_med3_f32 v89, v92, s61, v237
	v_med3_f32 v90, v93, s61, v237
	v_med3_f32 v83, v85, s61, v237
	v_cvt_pk_fp8_f32 v86, v89, v90 op_sel:[0,0,1]
	v_cvt_pk_fp8_f32 v87, v82, v83 op_sel:[0,0,1]


	v_mad_i64_i32 v[82:83], s[26:27], v107, s5, v[114:115]


	v_lshl_add_u64 v[82:83], v[82:83], 0, v[140:141]
	global_store_dwordx2 v[82:83], v[86:87], off
	v_mul_f32_e32 v82, 0xbfb8aa3b, v161
	v_pk_mul_f32 v[86:87], v[82:83], v[74:75] op_sel_hi:[0,1]
	v_pk_mul_f32 v[84:85], v[82:83], v[76:77] op_sel_hi:[0,1]
	v_pk_mul_f32 v[88:89], v[82:83], v[72:73] op_sel_hi:[0,1]
	v_pk_mul_f32 v[82:83], v[82:83], v[70:71] op_sel_hi:[0,1]
	v_exp_f32_e32 v86, v86
	v_exp_f32_e32 v87, v87
	v_exp_f32_e32 v82, v82
	v_exp_f32_e32 v83, v83
	v_exp_f32_e32 v88, v88
	v_exp_f32_e32 v89, v89
	v_pk_add_f32 v[86:87], v[86:87], 1.0 op_sel_hi:[1,0]


	v_exp_f32_e32 v84, v84
	v_exp_f32_e32 v85, v85
	v_pk_add_f32 v[88:89], v[88:89], 1.0 op_sel_hi:[1,0]
	v_pk_add_f32 v[82:83], v[82:83], 1.0 op_sel_hi:[1,0]
	v_rcp_f32_e32 v86, v86
	v_rcp_f32_e32 v87, v87


	v_rcp_f32_e32 v82, v82
	v_rcp_f32_e32 v83, v83
	v_rcp_f32_e32 v88, v88
	v_rcp_f32_e32 v89, v89
	v_or_b32_e32 v91, 48, v142
	v_mul_f32_e32 v90, v161, v161
	v_pk_add_f32 v[84:85], v[84:85], 1.0 op_sel_hi:[1,0]
	v_pk_mul_f32 v[74:75], v[74:75], v[78:79]
	v_pk_mul_f32 v[78:79], v[90:91], v[86:87] op_sel_hi:[0,1]


	v_rcp_f32_e32 v84, v84
	v_rcp_f32_e32 v85, v85
	v_pk_mul_f32 v[74:75], v[74:75], v[78:79]
	v_pk_mul_f32 v[66:67], v[70:71], v[66:67]
	v_pk_mul_f32 v[68:69], v[72:73], v[68:69]
	v_pk_mul_f32 v[70:71], v[90:91], v[82:83] op_sel_hi:[0,1]
	v_pk_mul_f32 v[72:73], v[90:91], v[88:89] op_sel_hi:[0,1]
	v_pk_mul_f32 v[68:69], v[68:69], v[72:73]
	v_pk_mul_f32 v[66:67], v[66:67], v[70:71]
	v_med3_f32 v71, v74, s61, v237
	v_med3_f32 v72, v75, s61, v237
	v_mov_b32_e32 v70, v1
	v_cvt_pk_fp8_f32 v70, v71, v72
	v_med3_f32 v66, v66, s61, v237
	v_med3_f32 v67, v67, s61, v237
	v_mov_b32_e32 v71, v1
	v_cvt_pk_fp8_f32 v71, v66, v67
	v_pk_mul_f32 v[76:77], v[76:77], v[80:81]
	v_pk_mul_f32 v[80:81], v[90:91], v[84:85] op_sel_hi:[0,1]
	v_pk_mul_f32 v[76:77], v[76:77], v[80:81]
	v_med3_f32 v66, v68, s61, v237
	v_med3_f32 v73, v76, s61, v237
	v_med3_f32 v74, v77, s61, v237
	v_med3_f32 v67, v69, s61, v237
	v_cvt_pk_fp8_f32 v70, v73, v74 op_sel:[0,0,1]
	v_cvt_pk_fp8_f32 v71, v66, v67 op_sel:[0,0,1]


	v_mad_i64_i32 v[66:67], s[26:27], v91, s5, v[114:115]


	v_mul_f32_e32 v149, 0x3a800000, v149
	v_lshl_add_u64 v[66:67], v[66:67], 0, v[140:141]
	global_store_dwordx2 v[66:67], v[70:71], off
	v_mul_f32_e32 v66, 0xbfb8aa3b, v149
	v_pk_mul_f32 v[70:71], v[66:67], v[58:59] op_sel_hi:[0,1]
	v_pk_mul_f32 v[68:69], v[66:67], v[60:61] op_sel_hi:[0,1]
	v_pk_mul_f32 v[72:73], v[66:67], v[56:57] op_sel_hi:[0,1]
	v_pk_mul_f32 v[66:67], v[66:67], v[54:55] op_sel_hi:[0,1]
	v_exp_f32_e32 v70, v70
	v_exp_f32_e32 v71, v71
	v_exp_f32_e32 v66, v66
	v_exp_f32_e32 v67, v67
	v_exp_f32_e32 v72, v72
	v_exp_f32_e32 v73, v73
	v_pk_add_f32 v[70:71], v[70:71], 1.0 op_sel_hi:[1,0]


	v_exp_f32_e32 v68, v68
	v_exp_f32_e32 v69, v69
	v_pk_add_f32 v[72:73], v[72:73], 1.0 op_sel_hi:[1,0]
	v_pk_add_f32 v[66:67], v[66:67], 1.0 op_sel_hi:[1,0]
	v_rcp_f32_e32 v70, v70
	v_rcp_f32_e32 v71, v71


	v_rcp_f32_e32 v66, v66
	v_rcp_f32_e32 v67, v67
	v_rcp_f32_e32 v72, v72
	v_rcp_f32_e32 v73, v73
	v_mul_f32_e32 v74, v149, v149
	v_pk_add_f32 v[68:69], v[68:69], 1.0 op_sel_hi:[1,0]
	v_pk_mul_f32 v[58:59], v[58:59], v[62:63]
	v_pk_mul_f32 v[62:63], v[74:75], v[70:71] op_sel_hi:[0,1]


	v_rcp_f32_e32 v68, v68
	v_rcp_f32_e32 v69, v69
	v_pk_mul_f32 v[58:59], v[58:59], v[62:63]
	v_pk_mul_f32 v[50:51], v[54:55], v[50:51]
	v_pk_mul_f32 v[52:53], v[56:57], v[52:53]
	v_pk_mul_f32 v[54:55], v[74:75], v[66:67] op_sel_hi:[0,1]
	v_pk_mul_f32 v[56:57], v[74:75], v[72:73] op_sel_hi:[0,1]
	v_pk_mul_f32 v[52:53], v[52:53], v[56:57]
	v_pk_mul_f32 v[50:51], v[50:51], v[54:55]
	v_med3_f32 v55, v58, s61, v237
	v_med3_f32 v56, v59, s61, v237
	v_mov_b32_e32 v54, v1
	v_cvt_pk_fp8_f32 v54, v55, v56
	v_med3_f32 v50, v50, s61, v237
	v_med3_f32 v51, v51, s61, v237
	v_mov_b32_e32 v55, v1
	v_cvt_pk_fp8_f32 v55, v50, v51
	v_pk_mul_f32 v[60:61], v[60:61], v[64:65]
	v_pk_mul_f32 v[64:65], v[74:75], v[68:69] op_sel_hi:[0,1]
	v_pk_mul_f32 v[60:61], v[60:61], v[64:65]
	v_med3_f32 v50, v52, s61, v237
	v_med3_f32 v57, v60, s61, v237
	v_med3_f32 v58, v61, s61, v237
	v_med3_f32 v51, v53, s61, v237
	v_cvt_pk_fp8_f32 v54, v57, v58 op_sel:[0,0,1]
	v_cvt_pk_fp8_f32 v55, v50, v51 op_sel:[0,0,1]
	v_add_u32_e32 v148, 0x80, v142


	v_mad_i64_i32 v[50:51], s[26:27], v148, s5, v[114:115]


	v_lshl_add_u64 v[50:51], v[50:51], 0, v[140:141]
	global_store_dwordx2 v[50:51], v[54:55], off
	v_mul_f32_e32 v50, 0xbfb8aa3b, v147
	v_pk_mul_f32 v[54:55], v[50:51], v[42:43] op_sel_hi:[0,1]
	v_pk_mul_f32 v[52:53], v[50:51], v[44:45] op_sel_hi:[0,1]
	v_pk_mul_f32 v[56:57], v[50:51], v[40:41] op_sel_hi:[0,1]
	v_pk_mul_f32 v[50:51], v[50:51], v[38:39] op_sel_hi:[0,1]
	v_exp_f32_e32 v54, v54
	v_exp_f32_e32 v55, v55
	v_exp_f32_e32 v50, v50
	v_exp_f32_e32 v51, v51
	v_exp_f32_e32 v56, v56
	v_exp_f32_e32 v57, v57
	v_pk_add_f32 v[54:55], v[54:55], 1.0 op_sel_hi:[1,0]


	v_exp_f32_e32 v52, v52
	v_exp_f32_e32 v53, v53
	v_pk_add_f32 v[56:57], v[56:57], 1.0 op_sel_hi:[1,0]
	v_pk_add_f32 v[50:51], v[50:51], 1.0 op_sel_hi:[1,0]
	v_rcp_f32_e32 v54, v54
	v_rcp_f32_e32 v55, v55


	v_rcp_f32_e32 v50, v50
	v_rcp_f32_e32 v51, v51
	v_rcp_f32_e32 v56, v56
	v_rcp_f32_e32 v57, v57
	v_add_u32_e32 v59, 0x90, v142
	v_mul_f32_e32 v58, v147, v147
	v_pk_add_f32 v[52:53], v[52:53], 1.0 op_sel_hi:[1,0]
	v_pk_mul_f32 v[42:43], v[42:43], v[46:47]
	v_pk_mul_f32 v[46:47], v[58:59], v[54:55] op_sel_hi:[0,1]


	v_rcp_f32_e32 v52, v52
	v_rcp_f32_e32 v53, v53
	v_pk_mul_f32 v[42:43], v[42:43], v[46:47]
	v_pk_mul_f32 v[34:35], v[38:39], v[34:35]
	v_pk_mul_f32 v[36:37], v[40:41], v[36:37]
	v_pk_mul_f32 v[38:39], v[58:59], v[50:51] op_sel_hi:[0,1]
	v_pk_mul_f32 v[40:41], v[58:59], v[56:57] op_sel_hi:[0,1]
	v_pk_mul_f32 v[36:37], v[36:37], v[40:41]
	v_pk_mul_f32 v[34:35], v[34:35], v[38:39]
	v_med3_f32 v39, v42, s61, v237
	v_med3_f32 v40, v43, s61, v237
	v_mov_b32_e32 v38, v1
	v_cvt_pk_fp8_f32 v38, v39, v40
	v_med3_f32 v34, v34, s61, v237
	v_med3_f32 v35, v35, s61, v237
	v_mov_b32_e32 v39, v1
	v_cvt_pk_fp8_f32 v39, v34, v35
	v_pk_mul_f32 v[44:45], v[44:45], v[48:49]
	v_pk_mul_f32 v[48:49], v[58:59], v[52:53] op_sel_hi:[0,1]
	v_pk_mul_f32 v[44:45], v[44:45], v[48:49]
	v_med3_f32 v34, v36, s61, v237
	v_med3_f32 v41, v44, s61, v237
	v_med3_f32 v42, v45, s61, v237
	v_med3_f32 v35, v37, s61, v237
	v_cvt_pk_fp8_f32 v38, v41, v42 op_sel:[0,0,1]
	v_cvt_pk_fp8_f32 v39, v34, v35 op_sel:[0,0,1]


	v_mad_i64_i32 v[34:35], s[26:27], v59, s5, v[114:115]


	v_lshl_add_u64 v[34:35], v[34:35], 0, v[140:141]
	global_store_dwordx2 v[34:35], v[38:39], off
	v_mul_f32_e32 v34, 0xbfb8aa3b, v146
	v_pk_mul_f32 v[38:39], v[34:35], v[26:27] op_sel_hi:[0,1]
	v_pk_mul_f32 v[36:37], v[34:35], v[28:29] op_sel_hi:[0,1]
	v_pk_mul_f32 v[40:41], v[34:35], v[24:25] op_sel_hi:[0,1]
	v_pk_mul_f32 v[34:35], v[34:35], v[22:23] op_sel_hi:[0,1]
	v_exp_f32_e32 v38, v38
	v_exp_f32_e32 v39, v39
	v_exp_f32_e32 v34, v34
	v_exp_f32_e32 v35, v35
	v_exp_f32_e32 v40, v40
	v_exp_f32_e32 v41, v41
	v_pk_add_f32 v[38:39], v[38:39], 1.0 op_sel_hi:[1,0]


	v_exp_f32_e32 v36, v36
	v_exp_f32_e32 v37, v37
	v_pk_add_f32 v[40:41], v[40:41], 1.0 op_sel_hi:[1,0]
	v_pk_add_f32 v[34:35], v[34:35], 1.0 op_sel_hi:[1,0]
	v_rcp_f32_e32 v38, v38
	v_rcp_f32_e32 v39, v39


	v_rcp_f32_e32 v34, v34
	v_rcp_f32_e32 v35, v35
	v_rcp_f32_e32 v40, v40
	v_rcp_f32_e32 v41, v41
	v_add_u32_e32 v43, 0xa0, v142
	v_mul_f32_e32 v42, v146, v146
	v_pk_add_f32 v[36:37], v[36:37], 1.0 op_sel_hi:[1,0]
	v_pk_mul_f32 v[26:27], v[26:27], v[30:31]
	v_pk_mul_f32 v[30:31], v[42:43], v[38:39] op_sel_hi:[0,1]


	v_rcp_f32_e32 v36, v36
	v_rcp_f32_e32 v37, v37
	v_pk_mul_f32 v[26:27], v[26:27], v[30:31]
	v_pk_mul_f32 v[18:19], v[22:23], v[18:19]
	v_pk_mul_f32 v[20:21], v[24:25], v[20:21]
	v_pk_mul_f32 v[22:23], v[42:43], v[34:35] op_sel_hi:[0,1]
	v_pk_mul_f32 v[24:25], v[42:43], v[40:41] op_sel_hi:[0,1]
	v_pk_mul_f32 v[20:21], v[20:21], v[24:25]
	v_pk_mul_f32 v[18:19], v[18:19], v[22:23]
	v_med3_f32 v23, v26, s61, v237
	v_med3_f32 v24, v27, s61, v237
	v_mov_b32_e32 v22, v1
	v_cvt_pk_fp8_f32 v22, v23, v24
	v_med3_f32 v18, v18, s61, v237
	v_med3_f32 v19, v19, s61, v237
	v_mov_b32_e32 v23, v1
	v_cvt_pk_fp8_f32 v23, v18, v19
	v_pk_mul_f32 v[28:29], v[28:29], v[32:33]
	v_pk_mul_f32 v[32:33], v[42:43], v[36:37] op_sel_hi:[0,1]
	v_pk_mul_f32 v[28:29], v[28:29], v[32:33]
	v_med3_f32 v18, v20, s61, v237
	v_med3_f32 v25, v28, s61, v237
	v_med3_f32 v26, v29, s61, v237
	v_med3_f32 v19, v21, s61, v237
	v_cvt_pk_fp8_f32 v22, v25, v26 op_sel:[0,0,1]
	v_cvt_pk_fp8_f32 v23, v18, v19 op_sel:[0,0,1]


	v_mad_i64_i32 v[18:19], s[26:27], v43, s5, v[114:115]


	v_lshl_add_u64 v[18:19], v[18:19], 0, v[140:141]
	global_store_dwordx2 v[18:19], v[22:23], off
	v_mul_f32_e32 v18, 0xbfb8aa3b, v143
	v_pk_mul_f32 v[22:23], v[18:19], v[10:11] op_sel_hi:[0,1]
	v_pk_mul_f32 v[20:21], v[18:19], v[12:13] op_sel_hi:[0,1]
	v_pk_mul_f32 v[24:25], v[18:19], v[8:9] op_sel_hi:[0,1]
	v_pk_mul_f32 v[18:19], v[18:19], v[6:7] op_sel_hi:[0,1]
	v_exp_f32_e32 v22, v22
	v_exp_f32_e32 v23, v23
	v_exp_f32_e32 v18, v18
	v_exp_f32_e32 v19, v19
	v_exp_f32_e32 v24, v24
	v_exp_f32_e32 v25, v25
	v_pk_add_f32 v[22:23], v[22:23], 1.0 op_sel_hi:[1,0]


	v_exp_f32_e32 v20, v20
	v_exp_f32_e32 v21, v21
	v_pk_add_f32 v[24:25], v[24:25], 1.0 op_sel_hi:[1,0]
	v_pk_add_f32 v[18:19], v[18:19], 1.0 op_sel_hi:[1,0]
	v_rcp_f32_e32 v22, v22
	v_rcp_f32_e32 v23, v23


	v_rcp_f32_e32 v18, v18
	v_rcp_f32_e32 v19, v19
	v_rcp_f32_e32 v24, v24
	v_rcp_f32_e32 v25, v25
	v_add_u32_e32 v27, 0xb0, v142
	v_mul_f32_e32 v26, v143, v143
	v_pk_add_f32 v[20:21], v[20:21], 1.0 op_sel_hi:[1,0]
	v_pk_mul_f32 v[10:11], v[10:11], v[14:15]
	v_pk_mul_f32 v[14:15], v[26:27], v[22:23] op_sel_hi:[0,1]


	v_rcp_f32_e32 v20, v20
	v_rcp_f32_e32 v21, v21
	v_pk_mul_f32 v[10:11], v[10:11], v[14:15]
	v_pk_mul_f32 v[2:3], v[6:7], v[2:3]
	v_pk_mul_f32 v[4:5], v[8:9], v[4:5]
	v_pk_mul_f32 v[6:7], v[26:27], v[18:19] op_sel_hi:[0,1]
	v_pk_mul_f32 v[8:9], v[26:27], v[24:25] op_sel_hi:[0,1]
	v_pk_mul_f32 v[4:5], v[4:5], v[8:9]
	v_pk_mul_f32 v[2:3], v[2:3], v[6:7]
	v_med3_f32 v7, v10, s61, v237
	v_med3_f32 v8, v11, s61, v237
	v_mov_b32_e32 v6, v1
	v_cvt_pk_fp8_f32 v6, v7, v8
	v_med3_f32 v2, v2, s61, v237
	v_med3_f32 v3, v3, s61, v237
	v_mov_b32_e32 v7, v1
	v_cvt_pk_fp8_f32 v7, v2, v3
	v_pk_mul_f32 v[12:13], v[12:13], v[16:17]
	v_pk_mul_f32 v[16:17], v[26:27], v[20:21] op_sel_hi:[0,1]
	v_pk_mul_f32 v[12:13], v[12:13], v[16:17]
	v_med3_f32 v2, v4, s61, v237
	v_med3_f32 v9, v12, s61, v237
	v_med3_f32 v10, v13, s61, v237
	v_med3_f32 v3, v5, s61, v237
	v_cvt_pk_fp8_f32 v6, v9, v10 op_sel:[0,0,1]
	v_cvt_pk_fp8_f32 v7, v2, v3 op_sel:[0,0,1]
	v_mad_i64_i32 v[2:3], s[26:27], v27, s5, v[114:115]
	v_lshl_add_u64 v[2:3], v[2:3], 0, v[140:141]
	s_andn2_b64 vcc, exec, s[18:19]
	s_mov_b64 s[18:19], -1
	s_mov_b32 s76, s55
	s_mov_b32 s77, s65
	global_store_dwordx2 v[2:3], v[6:7], off
	s_cbranch_vccnz .LBB0_1166
	s_andn2_b64 vcc, exec, s[8:9]
	s_cbranch_vccnz .LBB0_1165
	s_barrier
	s_branch .LBB0_1165

.LBB0_1376:
	v_cvt_f32_i32_e32 v123, v123
	v_cvt_f32_i32_e32 v122, v122
	v_cvt_f32_i32_e32 v125, v125
	v_cvt_f32_i32_e32 v124, v124
	v_cvt_f32_i32_e32 v119, v119
	v_cvt_f32_i32_e32 v118, v118
	v_cvt_f32_i32_e32 v121, v121
	v_cvt_f32_i32_e32 v120, v120
	v_cvt_f32_i32_e32 v127, v127
	v_cvt_f32_i32_e32 v126, v126
	v_cvt_f32_i32_e32 v129, v129
	v_cvt_f32_i32_e32 v128, v128
	s_waitcnt vmcnt(0)
	v_mul_f32_e32 v164, 0x3a800000, v141
	v_mul_f32_e32 v152, 0xbfb8aa3b, v164
	v_pk_mul_f32 v[156:157], v[152:153], v[122:123] op_sel_hi:[0,1]
	v_pk_mul_f32 v[154:155], v[152:153], v[124:125] op_sel_hi:[0,1]
	v_pk_mul_f32 v[158:159], v[152:153], v[120:121] op_sel_hi:[0,1]
	v_pk_mul_f32 v[152:153], v[152:153], v[118:119] op_sel_hi:[0,1]
	v_exp_f32_e32 v156, v156
	v_exp_f32_e32 v157, v157
	v_exp_f32_e32 v152, v152
	v_exp_f32_e32 v153, v153
	v_exp_f32_e32 v154, v154
	v_exp_f32_e32 v155, v155
	s_mul_hi_i32 s4, s44, 0x2e8ba2e9
	v_exp_f32_e32 v158, v158
	v_exp_f32_e32 v159, v159
	s_lshr_b32 s5, s4, 31
	s_lshr_b32 s4, s4, 2
	s_add_i32 s4, s4, s5
	v_cvt_f32_i32_e32 v161, v117
	v_cvt_f32_i32_e32 v160, v116
	v_pk_add_f32 v[116:117], v[156:157], 1.0 op_sel_hi:[1,0]
	s_mul_i32 s4, s4, 22


	v_cvt_f32_i32_e32 v163, v115
	v_cvt_f32_i32_e32 v162, v114
	v_pk_add_f32 v[114:115], v[154:155], 1.0 op_sel_hi:[1,0]
	v_pk_add_f32 v[152:153], v[152:153], 1.0 op_sel_hi:[1,0]
	v_rcp_f32_e32 v116, v116
	v_rcp_f32_e32 v117, v117
	s_sub_i32 s4, s44, s4


	v_pk_add_f32 v[154:155], v[158:159], 1.0 op_sel_hi:[1,0]
	v_rcp_f32_e32 v152, v152
	v_rcp_f32_e32 v153, v153
	v_rcp_f32_e32 v114, v114
	v_rcp_f32_e32 v115, v115
	v_ashrrev_i32_e32 v140, 1, v140
	s_lshl_b32 s4, s4, 7
	v_rcp_f32_e32 v154, v154
	v_rcp_f32_e32 v155, v155
	v_and_b32_e32 v140, -8, v140
	s_or_b32 s4, s4, s41
	v_mul_f32_e32 v156, v164, v164
	v_add_u32_e32 v140, s4, v140
	v_pk_mul_f32 v[122:123], v[122:123], v[126:127]
	v_pk_mul_f32 v[116:117], v[156:157], v[116:117] op_sel_hi:[0,1]
	v_readlane_b32 s4, v255, 23
	v_pk_mul_f32 v[124:125], v[124:125], v[128:129]
	v_pk_mul_f32 v[114:115], v[156:157], v[114:115] op_sel_hi:[0,1]
	v_pk_mul_f32 v[116:117], v[122:123], v[116:117]
	v_pk_mul_f32 v[122:123], v[118:119], v[162:163]
	v_pk_mul_f32 v[118:119], v[120:121], v[160:161]
	v_pk_mul_f32 v[120:121], v[156:157], v[152:153] op_sel_hi:[0,1]
	v_readlane_b32 s5, v255, 24
	v_pk_mul_f32 v[114:115], v[124:125], v[114:115]
	v_pk_mul_f32 v[124:125], v[156:157], v[154:155] op_sel_hi:[0,1]
	v_pk_mul_f32 v[120:121], v[122:123], v[120:121]
	v_cndmask_b32_e64 v122, 0, 1, s[4:5]
	v_readlane_b32 s62, v255, 11
	v_readlane_b32 s78, v255, 13
	v_ashrrev_i32_e32 v141, 31, v140
	v_pk_mul_f32 v[118:119], v[118:119], v[124:125]
	v_cmp_ne_u32_e64 s[10:11], 1, v122
	s_andn2_b64 vcc, exec, s[4:5]
	s_mov_b64 s[26:27], -1
	v_readlane_b32 s63, v255, 12
	v_readlane_b32 s79, v255, 14
	s_movk_i32 s19, 0xb00
	s_movk_i32 s21, 0x1600
	s_movk_i32 s74, 0x1000
	s_cbranch_vccnz .LBB0_1378
	v_max_f32_e32 v122, v116, v116
	v_med3_f32 v123, v122, s61, v237
	v_max_f32_e32 v122, v117, v117
	v_med3_f32 v124, v122, s61, v237
	v_mov_b32_e32 v122, v1
	v_cvt_pk_fp8_f32 v122, v123, v124
	v_max_f32_e32 v125, v114, v114
	v_max_f32_e32 v124, v115, v115
	v_med3_f32 v123, v125, s61, v237
	v_med3_f32 v124, v124, s61, v237
	v_cvt_pk_fp8_f32 v122, v123, v124 op_sel:[0,0,1]
	v_max_f32_e32 v123, v120, v120
	v_med3_f32 v124, v123, s61, v237
	v_max_f32_e32 v123, v121, v121
	v_med3_f32 v125, v123, s61, v237
	v_mov_b32_e32 v123, v1
	v_cvt_pk_fp8_f32 v123, v124, v125
	v_max_f32_e32 v126, v118, v118
	v_max_f32_e32 v125, v119, v119
	v_med3_f32 v124, v126, s61, v237
	v_med3_f32 v125, v125, s61, v237
	v_cvt_pk_fp8_f32 v123, v124, v125 op_sel:[0,0,1]
	v_mov_b64_e32 v[124:125], s[12:13]
	v_mad_i64_i32 v[124:125], s[4:5], v142, s19, v[124:125]
	v_lshl_add_u64 v[124:125], v[124:125], 0, v[140:141]
	s_mov_b64 s[26:27], 0
	global_store_dwordx2 v[124:125], v[122:123], off
